# v29 + nt on the P6 epilogue residual (x) loads: streamed once, keeps GEMM operand panels in L2
# baseline (speedup 1.0000x reference)
.LBB0_934:
	s_ashr_i32 s3, s97, 31
	s_lshr_b32 s3, s3, 26
	s_add_i32 s3, s97, s3
	s_and_b32 s3, s3, 0xffffc0
	s_sub_i32 s3, s97, s3
	s_lshl_b32 s3, s3, 8
	v_readlane_b32 s4, v249, 5
	s_add_i32 s3, s3, s4
	s_nop 15
	s_nop 15
	v_mbcnt_lo_u32_b32 v0, -1, 0
	v_mbcnt_hi_u32_b32 v0, -1, v0
	s_nop 0
	v_and_or_b32 v36, v0, 15, s3
	s_lshl_b32 s3, s96, 8
	v_and_b32_e32 v0, -16, v0
	s_or_b32 s3, s3, s88
	v_add_u32_e32 v32, s3, v0
	v_ashrrev_i32_e32 v33, 31, v32
	v_lshlrev_b64 v[34:35], 1, v[32:33]
	v_ashrrev_i32_e32 v37, 31, v36
	v_or_b32_e32 v40, 16, v36
	v_lshl_add_u64 v[38:39], s[44:45], 0, v[34:35]
	v_lshlrev_b64 v[192:193], 13, v[36:37]
	v_ashrrev_i32_e32 v41, 31, v40
	v_or_b32_e32 v44, 32, v36
	v_or_b32_e32 v196, 48, v36
	v_lshl_add_u64 v[12:13], v[32:33], 2, s[50:51]
	v_lshl_add_u64 v[16:17], v[38:39], 0, v[192:193]
	v_lshlrev_b64 v[194:195], 13, v[40:41]
	v_ashrrev_i32_e32 v45, 31, v44
	v_ashrrev_i32_e32 v197, 31, v196
	global_load_dwordx4 v[0:3], v[12:13], off offset:48
	global_load_dwordx4 v[4:7], v[12:13], off offset:32
	global_load_dwordx4 v[8:11], v[12:13], off offset:16
	s_nop 0
	global_load_dwordx4 v[12:15], v[12:13], off
	s_nop 0
	global_load_dwordx4 v[48:51], v[16:17], off offset:16 nt
	global_load_dwordx4 v[52:55], v[16:17], off nt
	v_lshl_add_u64 v[16:17], v[38:39], 0, v[194:195]
	v_lshlrev_b64 v[46:47], 13, v[44:45]
	v_lshlrev_b64 v[42:43], 13, v[196:197]
	global_load_dwordx4 v[56:59], v[16:17], off offset:16 nt
	global_load_dwordx4 v[60:63], v[16:17], off nt
	v_lshl_add_u64 v[16:17], v[38:39], 0, v[46:47]
	v_lshl_add_u64 v[20:21], v[38:39], 0, v[42:43]
	global_load_dwordx4 v[24:27], v[16:17], off offset:16 nt
	global_load_dwordx4 v[28:31], v[16:17], off nt
	s_nop 0
	global_load_dwordx4 v[16:19], v[20:21], off offset:16 nt
	s_nop 0
	global_load_dwordx4 v[20:23], v[20:21], off nt
	v_lshl_add_u64 v[34:35], s[40:41], 0, v[34:35]
	v_lshlrev_b64 v[198:199], 12, v[36:37]
	v_lshlrev_b64 v[222:223], 12, v[40:41]
	v_lshlrev_b64 v[44:45], 12, v[44:45]
	v_lshlrev_b64 v[40:41], 12, v[196:197]
	s_waitcnt vmcnt(6)
	v_lshlrev_b32_e32 v196, 16, v52
	v_and_b32_e32 v197, 0xffff0000, v52
	v_lshlrev_b32_e32 v52, 16, v53
	v_and_b32_e32 v53, 0xffff0000, v53
	v_pk_fma_f32 v[224:225], v[190:191], s[46:47], v[52:53] op_sel_hi:[1,0,1]
	v_lshlrev_b32_e32 v52, 16, v54
	v_and_b32_e32 v53, 0xffff0000, v54
	v_lshlrev_b32_e32 v54, 16, v55
	v_and_b32_e32 v55, 0xffff0000, v55
	v_pk_fma_f32 v[196:197], v[188:189], s[46:47], v[196:197] op_sel_hi:[1,0,1]
	v_pk_fma_f32 v[226:227], v[186:187], s[46:47], v[54:55] op_sel_hi:[1,0,1]
	v_pk_fma_f32 v[228:229], v[184:185], s[46:47], v[52:53] op_sel_hi:[1,0,1]
	v_cvt_pk_bf16_f32 v52, v196, v197
	v_cvt_pk_bf16_f32 v55, v226, v227
	v_lshl_add_u64 v[192:193], v[34:35], 0, v[192:193]
	v_cvt_pk_bf16_f32 v54, v228, v229
	v_cvt_pk_bf16_f32 v53, v224, v225
	global_store_dwordx4 v[192:193], v[52:55], off
	v_lshl_add_u64 v[46:47], v[34:35], 0, v[46:47]
	v_lshl_add_u64 v[42:43], v[34:35], 0, v[42:43]
	v_pk_mul_f32 v[54:55], v[12:13], v[196:197]
	v_mov_b32_e32 v52, v203
	v_pk_mul_f32 v[196:197], v[8:9], v[228:229]
	v_cvt_pk_fp8_f32 v52, v54, v55
	v_mov_b32_e32 v53, v203
	v_cvt_pk_fp8_f32 v53, v196, v197
	v_pk_mul_f32 v[54:55], v[14:15], v[224:225]
	v_pk_mul_f32 v[196:197], v[10:11], v[226:227]
	v_cvt_pk_fp8_f32 v52, v54, v55 op_sel:[0,0,1]
	v_lshlrev_b32_e32 v54, 16, v48
	v_and_b32_e32 v55, 0xffff0000, v48
	v_lshlrev_b32_e32 v48, 16, v49
	v_and_b32_e32 v49, 0xffff0000, v49
	v_cvt_pk_fp8_f32 v53, v196, v197 op_sel:[0,0,1]
	v_pk_fma_f32 v[196:197], v[158:159], s[46:47], v[48:49] op_sel_hi:[1,0,1]
	v_lshlrev_b32_e32 v48, 16, v50
	v_and_b32_e32 v49, 0xffff0000, v50
	v_pk_fma_f32 v[54:55], v[156:157], s[46:47], v[54:55] op_sel_hi:[1,0,1]
	v_lshlrev_b32_e32 v50, 16, v51
	v_and_b32_e32 v51, 0xffff0000, v51
	v_pk_fma_f32 v[226:227], v[152:153], s[46:47], v[48:49] op_sel_hi:[1,0,1]
	v_pk_fma_f32 v[224:225], v[154:155], s[46:47], v[50:51] op_sel_hi:[1,0,1]
	v_cvt_pk_bf16_f32 v48, v54, v55
	v_cvt_pk_bf16_f32 v50, v226, v227
	v_pk_mul_f32 v[228:229], v[4:5], v[54:55]
	v_pk_mul_f32 v[226:227], v[0:1], v[226:227]
	v_mov_b32_e32 v54, v203
	v_mov_b32_e32 v55, v203
	v_cvt_pk_fp8_f32 v54, v228, v229
	v_cvt_pk_fp8_f32 v55, v226, v227
	v_cvt_pk_bf16_f32 v49, v196, v197
	v_cvt_pk_bf16_f32 v51, v224, v225
	v_pk_mul_f32 v[196:197], v[6:7], v[196:197]
	v_pk_mul_f32 v[224:225], v[2:3], v[224:225]
	v_cvt_pk_fp8_f32 v54, v196, v197 op_sel:[0,0,1]
	v_cvt_pk_fp8_f32 v55, v224, v225 op_sel:[0,0,1]
	global_store_dwordx4 v[192:193], v[48:51], off offset:16
	v_lshl_add_u64 v[192:193], v[34:35], 0, v[194:195]
	s_nop 0
	v_lshl_add_u64 v[48:49], s[42:43], 0, v[198:199]
	v_lshl_add_u64 v[48:49], v[48:49], 0, v[32:33]
	global_store_dwordx4 v[48:49], v[52:55], off
	s_waitcnt vmcnt(7)
	v_lshlrev_b32_e32 v48, 16, v60
	v_and_b32_e32 v49, 0xffff0000, v60
	v_lshlrev_b32_e32 v50, 16, v61
	v_and_b32_e32 v51, 0xffff0000, v61
	v_pk_fma_f32 v[52:53], v[182:183], s[46:47], v[50:51] op_sel_hi:[1,0,1]
	v_pk_fma_f32 v[54:55], v[180:181], s[46:47], v[48:49] op_sel_hi:[1,0,1]
	v_lshlrev_b32_e32 v48, 16, v62
	v_and_b32_e32 v49, 0xffff0000, v62
	v_lshlrev_b32_e32 v50, 16, v63
	v_and_b32_e32 v51, 0xffff0000, v63
	v_pk_fma_f32 v[60:61], v[178:179], s[46:47], v[50:51] op_sel_hi:[1,0,1]
	v_pk_fma_f32 v[62:63], v[176:177], s[46:47], v[48:49] op_sel_hi:[1,0,1]
	v_cvt_pk_bf16_f32 v49, v52, v53
	v_cvt_pk_bf16_f32 v51, v60, v61
	v_cvt_pk_bf16_f32 v48, v54, v55
	s_nop 0
	v_cvt_pk_bf16_f32 v50, v62, v63
	global_store_dwordx4 v[192:193], v[48:51], off
	s_nop 1
	v_pk_mul_f32 v[50:51], v[12:13], v[54:55]
	v_pk_mul_f32 v[54:55], v[8:9], v[62:63]
	v_mov_b32_e32 v49, v203
	v_mov_b32_e32 v48, v203
	v_cvt_pk_fp8_f32 v49, v54, v55
	v_cvt_pk_fp8_f32 v48, v50, v51
	v_pk_mul_f32 v[50:51], v[14:15], v[52:53]
	v_pk_mul_f32 v[52:53], v[10:11], v[60:61]
	v_lshlrev_b32_e32 v54, 16, v59
	v_cvt_pk_fp8_f32 v49, v52, v53 op_sel:[0,0,1]
	v_lshlrev_b32_e32 v52, 16, v57
	v_and_b32_e32 v53, 0xffff0000, v57
	v_cvt_pk_fp8_f32 v48, v50, v51 op_sel:[0,0,1]
	v_lshlrev_b32_e32 v50, 16, v56
	v_and_b32_e32 v51, 0xffff0000, v56
	v_pk_fma_f32 v[56:57], v[150:151], s[46:47], v[52:53] op_sel_hi:[1,0,1]
	v_lshlrev_b32_e32 v52, 16, v58
	v_and_b32_e32 v53, 0xffff0000, v58
	v_pk_fma_f32 v[50:51], v[148:149], s[46:47], v[50:51] op_sel_hi:[1,0,1]
	v_and_b32_e32 v55, 0xffff0000, v59
	v_pk_fma_f32 v[60:61], v[144:145], s[46:47], v[52:53] op_sel_hi:[1,0,1]
	v_pk_fma_f32 v[58:59], v[146:147], s[46:47], v[54:55] op_sel_hi:[1,0,1]
	v_cvt_pk_bf16_f32 v52, v50, v51
	v_cvt_pk_bf16_f32 v54, v60, v61
	v_pk_mul_f32 v[62:63], v[4:5], v[50:51]
	v_pk_mul_f32 v[60:61], v[0:1], v[60:61]
	v_mov_b32_e32 v50, v203
	v_mov_b32_e32 v51, v203
	v_cvt_pk_fp8_f32 v50, v62, v63
	v_cvt_pk_fp8_f32 v51, v60, v61
	v_cvt_pk_bf16_f32 v53, v56, v57
	v_cvt_pk_bf16_f32 v55, v58, v59
	v_pk_mul_f32 v[56:57], v[6:7], v[56:57]
	v_pk_mul_f32 v[58:59], v[2:3], v[58:59]
	v_cvt_pk_fp8_f32 v50, v56, v57 op_sel:[0,0,1]
	v_cvt_pk_fp8_f32 v51, v58, v59 op_sel:[0,0,1]
	global_store_dwordx4 v[192:193], v[52:55], off offset:16
	s_nop 1
	v_lshl_add_u64 v[52:53], s[42:43], 0, v[222:223]
	v_lshl_add_u64 v[52:53], v[52:53], 0, v[32:33]
	global_store_dwordx4 v[52:53], v[48:51], off
	s_waitcnt vmcnt(8)
	s_nop 0
	v_lshlrev_b32_e32 v48, 16, v28
	v_and_b32_e32 v49, 0xffff0000, v28
	v_lshlrev_b32_e32 v28, 16, v29
	v_and_b32_e32 v29, 0xffff0000, v29
	v_pk_fma_f32 v[50:51], v[174:175], s[46:47], v[28:29] op_sel_hi:[1,0,1]
	v_lshlrev_b32_e32 v28, 16, v30
	v_and_b32_e32 v29, 0xffff0000, v30
	v_lshlrev_b32_e32 v30, 16, v31
	v_and_b32_e32 v31, 0xffff0000, v31
	v_pk_fma_f32 v[48:49], v[172:173], s[46:47], v[48:49] op_sel_hi:[1,0,1]
	v_pk_fma_f32 v[52:53], v[170:171], s[46:47], v[30:31] op_sel_hi:[1,0,1]
	v_pk_fma_f32 v[54:55], v[168:169], s[46:47], v[28:29] op_sel_hi:[1,0,1]
	v_cvt_pk_bf16_f32 v28, v48, v49
	v_cvt_pk_bf16_f32 v31, v52, v53
	v_cvt_pk_bf16_f32 v29, v50, v51
	s_nop 0
	v_cvt_pk_bf16_f32 v30, v54, v55
	global_store_dwordx4 v[46:47], v[28:31], off
	s_nop 1
	v_pk_mul_f32 v[30:31], v[12:13], v[48:49]
	v_mov_b32_e32 v28, v203
	v_pk_mul_f32 v[48:49], v[8:9], v[54:55]
	v_cvt_pk_fp8_f32 v28, v30, v31
	v_mov_b32_e32 v29, v203
	v_cvt_pk_fp8_f32 v29, v48, v49
	v_pk_mul_f32 v[30:31], v[14:15], v[50:51]
	v_pk_mul_f32 v[48:49], v[10:11], v[52:53]
	v_cvt_pk_fp8_f32 v28, v30, v31 op_sel:[0,0,1]
	v_lshlrev_b32_e32 v30, 16, v24
	v_and_b32_e32 v31, 0xffff0000, v24
	v_lshlrev_b32_e32 v24, 16, v25
	v_and_b32_e32 v25, 0xffff0000, v25
	v_cvt_pk_fp8_f32 v29, v48, v49 op_sel:[0,0,1]
	v_pk_fma_f32 v[48:49], v[142:143], s[46:47], v[24:25] op_sel_hi:[1,0,1]
	v_lshlrev_b32_e32 v24, 16, v26
	v_and_b32_e32 v25, 0xffff0000, v26
	v_pk_fma_f32 v[30:31], v[140:141], s[46:47], v[30:31] op_sel_hi:[1,0,1]
	v_lshlrev_b32_e32 v26, 16, v27
	v_and_b32_e32 v27, 0xffff0000, v27
	v_pk_fma_f32 v[52:53], v[136:137], s[46:47], v[24:25] op_sel_hi:[1,0,1]
	v_pk_fma_f32 v[50:51], v[138:139], s[46:47], v[26:27] op_sel_hi:[1,0,1]
	v_cvt_pk_bf16_f32 v24, v30, v31
	v_cvt_pk_bf16_f32 v26, v52, v53
	v_pk_mul_f32 v[54:55], v[4:5], v[30:31]
	v_pk_mul_f32 v[52:53], v[0:1], v[52:53]
	v_mov_b32_e32 v30, v203
	v_mov_b32_e32 v31, v203
	v_cvt_pk_fp8_f32 v30, v54, v55
	v_cvt_pk_fp8_f32 v31, v52, v53
	v_cvt_pk_bf16_f32 v25, v48, v49
	v_cvt_pk_bf16_f32 v27, v50, v51
	v_pk_mul_f32 v[48:49], v[6:7], v[48:49]
	v_pk_mul_f32 v[50:51], v[2:3], v[50:51]
	v_cvt_pk_fp8_f32 v30, v48, v49 op_sel:[0,0,1]
	v_cvt_pk_fp8_f32 v31, v50, v51 op_sel:[0,0,1]
	global_store_dwordx4 v[46:47], v[24:27], off offset:16
	s_nop 1
	v_lshl_add_u64 v[24:25], s[42:43], 0, v[44:45]
	v_lshl_add_u64 v[24:25], v[24:25], 0, v[32:33]
	global_store_dwordx4 v[24:25], v[28:31], off
	s_waitcnt vmcnt(9)
	v_lshlrev_b32_e32 v24, 16, v20
	v_and_b32_e32 v25, 0xffff0000, v20
	v_lshlrev_b32_e32 v20, 16, v21
	v_and_b32_e32 v21, 0xffff0000, v21
	v_pk_fma_f32 v[26:27], v[166:167], s[46:47], v[20:21] op_sel_hi:[1,0,1]
	v_lshlrev_b32_e32 v20, 16, v22
	v_and_b32_e32 v21, 0xffff0000, v22
	v_lshlrev_b32_e32 v22, 16, v23
	v_and_b32_e32 v23, 0xffff0000, v23
	v_pk_fma_f32 v[24:25], v[164:165], s[46:47], v[24:25] op_sel_hi:[1,0,1]
	v_pk_fma_f32 v[28:29], v[162:163], s[46:47], v[22:23] op_sel_hi:[1,0,1]
	v_pk_fma_f32 v[30:31], v[160:161], s[46:47], v[20:21] op_sel_hi:[1,0,1]
	v_cvt_pk_bf16_f32 v20, v24, v25
	v_cvt_pk_bf16_f32 v23, v28, v29
	v_cvt_pk_bf16_f32 v21, v26, v27
	s_nop 0
	v_cvt_pk_bf16_f32 v22, v30, v31
	global_store_dwordx4 v[42:43], v[20:23], off
	s_nop 1
	v_pk_mul_f32 v[22:23], v[12:13], v[24:25]
	v_mov_b32_e32 v20, v203
	v_pk_mul_f32 v[24:25], v[8:9], v[30:31]
	v_cvt_pk_fp8_f32 v20, v22, v23
	v_mov_b32_e32 v21, v203
	v_cvt_pk_fp8_f32 v21, v24, v25
	v_pk_mul_f32 v[22:23], v[14:15], v[26:27]
	v_pk_mul_f32 v[24:25], v[10:11], v[28:29]
	v_cvt_pk_fp8_f32 v20, v22, v23 op_sel:[0,0,1]
	v_lshlrev_b32_e32 v22, 16, v16
	v_and_b32_e32 v23, 0xffff0000, v16
	v_lshlrev_b32_e32 v16, 16, v17
	v_and_b32_e32 v17, 0xffff0000, v17
	v_cvt_pk_fp8_f32 v21, v24, v25 op_sel:[0,0,1]
	v_pk_fma_f32 v[24:25], v[134:135], s[46:47], v[16:17] op_sel_hi:[1,0,1]
	v_lshlrev_b32_e32 v16, 16, v18
	v_and_b32_e32 v17, 0xffff0000, v18
	v_pk_fma_f32 v[22:23], v[132:133], s[46:47], v[22:23] op_sel_hi:[1,0,1]
	v_lshlrev_b32_e32 v18, 16, v19
	v_and_b32_e32 v19, 0xffff0000, v19
	v_pk_fma_f32 v[28:29], v[128:129], s[46:47], v[16:17] op_sel_hi:[1,0,1]
	v_pk_fma_f32 v[26:27], v[130:131], s[46:47], v[18:19] op_sel_hi:[1,0,1]
	v_cvt_pk_bf16_f32 v16, v22, v23
	v_cvt_pk_bf16_f32 v18, v28, v29
	v_pk_mul_f32 v[30:31], v[4:5], v[22:23]
	v_pk_mul_f32 v[28:29], v[0:1], v[28:29]
	v_mov_b32_e32 v22, v203
	v_mov_b32_e32 v23, v203
	v_cvt_pk_fp8_f32 v22, v30, v31
	v_cvt_pk_fp8_f32 v23, v28, v29
	v_cvt_pk_bf16_f32 v17, v24, v25
	v_cvt_pk_bf16_f32 v19, v26, v27
	v_pk_mul_f32 v[24:25], v[6:7], v[24:25]
	v_pk_mul_f32 v[26:27], v[2:3], v[26:27]
	v_cvt_pk_fp8_f32 v22, v24, v25 op_sel:[0,0,1]
	v_cvt_pk_fp8_f32 v23, v26, v27 op_sel:[0,0,1]
	global_store_dwordx4 v[42:43], v[16:19], off offset:16
	s_nop 1
	v_lshl_add_u64 v[16:17], s[42:43], 0, v[40:41]
	v_lshl_add_u64 v[16:17], v[16:17], 0, v[32:33]
	global_store_dwordx4 v[16:17], v[20:23], off
	v_add_u32_e32 v60, 0x80, v36
	v_ashrrev_i32_e32 v61, 31, v60
	v_add_u32_e32 v192, 0x90, v36
	v_lshlrev_b64 v[62:63], 13, v[60:61]
	v_ashrrev_i32_e32 v193, 31, v192
	v_add_u32_e32 v196, 0xa0, v36
	v_add_u32_e32 v36, 0xb0, v36
	v_lshl_add_u64 v[16:17], v[38:39], 0, v[62:63]
	v_lshlrev_b64 v[194:195], 13, v[192:193]
	v_ashrrev_i32_e32 v197, 31, v196
	v_ashrrev_i32_e32 v37, 31, v36
	global_load_dwordx4 v[44:47], v[16:17], off offset:16 nt
	global_load_dwordx4 v[48:51], v[16:17], off nt
	v_lshl_add_u64 v[16:17], v[38:39], 0, v[194:195]
	v_lshlrev_b64 v[42:43], 13, v[196:197]
	v_lshlrev_b64 v[40:41], 13, v[36:37]
	global_load_dwordx4 v[52:55], v[16:17], off offset:16 nt
	global_load_dwordx4 v[56:59], v[16:17], off nt
	v_lshl_add_u64 v[16:17], v[38:39], 0, v[42:43]
	v_lshl_add_u64 v[20:21], v[38:39], 0, v[40:41]
	global_load_dwordx4 v[24:27], v[16:17], off offset:16 nt
	global_load_dwordx4 v[28:31], v[16:17], off nt
	s_nop 0
	global_load_dwordx4 v[16:19], v[20:21], off offset:16 nt
	s_nop 0
	global_load_dwordx4 v[20:23], v[20:21], off nt
	v_lshlrev_b64 v[60:61], 12, v[60:61]
	v_lshlrev_b64 v[192:193], 12, v[192:193]
	v_lshlrev_b64 v[38:39], 12, v[196:197]
	v_lshlrev_b64 v[36:37], 12, v[36:37]
	s_waitcnt vmcnt(6)
	v_lshlrev_b32_e32 v196, 16, v48
	v_and_b32_e32 v197, 0xffff0000, v48
	v_lshlrev_b32_e32 v48, 16, v49
	v_and_b32_e32 v49, 0xffff0000, v49
	v_pk_fma_f32 v[198:199], v[126:127], s[46:47], v[48:49] op_sel_hi:[1,0,1]
	v_lshlrev_b32_e32 v48, 16, v50
	v_and_b32_e32 v49, 0xffff0000, v50
	v_lshlrev_b32_e32 v50, 16, v51
	v_and_b32_e32 v51, 0xffff0000, v51
	v_pk_fma_f32 v[196:197], v[124:125], s[46:47], v[196:197] op_sel_hi:[1,0,1]
	v_pk_fma_f32 v[222:223], v[122:123], s[46:47], v[50:51] op_sel_hi:[1,0,1]
	v_pk_fma_f32 v[224:225], v[120:121], s[46:47], v[48:49] op_sel_hi:[1,0,1]
	v_cvt_pk_bf16_f32 v48, v196, v197
	v_cvt_pk_bf16_f32 v51, v222, v223
	v_lshl_add_u64 v[62:63], v[34:35], 0, v[62:63]
	v_cvt_pk_bf16_f32 v50, v224, v225
	v_cvt_pk_bf16_f32 v49, v198, v199
	global_store_dwordx4 v[62:63], v[48:51], off
	v_lshl_add_u64 v[42:43], v[34:35], 0, v[42:43]
	s_nop 0
	v_pk_mul_f32 v[50:51], v[12:13], v[196:197]
	v_mov_b32_e32 v48, v203
	v_pk_mul_f32 v[196:197], v[8:9], v[224:225]
	v_cvt_pk_fp8_f32 v48, v50, v51
	v_mov_b32_e32 v49, v203
	v_cvt_pk_fp8_f32 v49, v196, v197
	v_pk_mul_f32 v[50:51], v[14:15], v[198:199]
	v_pk_mul_f32 v[196:197], v[10:11], v[222:223]
	v_cvt_pk_fp8_f32 v48, v50, v51 op_sel:[0,0,1]
	v_lshlrev_b32_e32 v50, 16, v44
	v_and_b32_e32 v51, 0xffff0000, v44
	v_lshlrev_b32_e32 v44, 16, v45
	v_and_b32_e32 v45, 0xffff0000, v45
	v_cvt_pk_fp8_f32 v49, v196, v197 op_sel:[0,0,1]
	v_pk_fma_f32 v[196:197], v[94:95], s[46:47], v[44:45] op_sel_hi:[1,0,1]
	v_lshlrev_b32_e32 v44, 16, v46
	v_and_b32_e32 v45, 0xffff0000, v46
	v_pk_fma_f32 v[50:51], v[92:93], s[46:47], v[50:51] op_sel_hi:[1,0,1]
	v_lshlrev_b32_e32 v46, 16, v47
	v_and_b32_e32 v47, 0xffff0000, v47
	v_pk_fma_f32 v[222:223], v[88:89], s[46:47], v[44:45] op_sel_hi:[1,0,1]
	v_pk_fma_f32 v[198:199], v[90:91], s[46:47], v[46:47] op_sel_hi:[1,0,1]
	v_cvt_pk_bf16_f32 v44, v50, v51
	v_cvt_pk_bf16_f32 v46, v222, v223
	v_pk_mul_f32 v[224:225], v[4:5], v[50:51]
	v_pk_mul_f32 v[222:223], v[0:1], v[222:223]
	v_mov_b32_e32 v50, v203
	v_mov_b32_e32 v51, v203
	v_cvt_pk_fp8_f32 v50, v224, v225
	v_cvt_pk_fp8_f32 v51, v222, v223
	v_cvt_pk_bf16_f32 v45, v196, v197
	v_cvt_pk_bf16_f32 v47, v198, v199
	v_pk_mul_f32 v[196:197], v[6:7], v[196:197]
	v_pk_mul_f32 v[198:199], v[2:3], v[198:199]
	v_cvt_pk_fp8_f32 v50, v196, v197 op_sel:[0,0,1]
	v_cvt_pk_fp8_f32 v51, v198, v199 op_sel:[0,0,1]
	global_store_dwordx4 v[62:63], v[44:47], off offset:16
	s_nop 1
	v_lshl_add_u64 v[44:45], s[42:43], 0, v[60:61]
	v_lshl_add_u64 v[44:45], v[44:45], 0, v[32:33]
	global_store_dwordx4 v[44:45], v[48:51], off
	s_waitcnt vmcnt(7)
	v_lshlrev_b32_e32 v44, 16, v56
	v_and_b32_e32 v45, 0xffff0000, v56
	v_lshlrev_b32_e32 v46, 16, v57
	v_and_b32_e32 v47, 0xffff0000, v57
	v_pk_fma_f32 v[48:49], v[118:119], s[46:47], v[46:47] op_sel_hi:[1,0,1]
	v_pk_fma_f32 v[50:51], v[116:117], s[46:47], v[44:45] op_sel_hi:[1,0,1]
	v_lshlrev_b32_e32 v44, 16, v58
	v_and_b32_e32 v45, 0xffff0000, v58
	v_lshlrev_b32_e32 v46, 16, v59
	v_and_b32_e32 v47, 0xffff0000, v59
	v_pk_fma_f32 v[56:57], v[114:115], s[46:47], v[46:47] op_sel_hi:[1,0,1]
	v_pk_fma_f32 v[58:59], v[112:113], s[46:47], v[44:45] op_sel_hi:[1,0,1]
	v_cvt_pk_bf16_f32 v45, v48, v49
	v_cvt_pk_bf16_f32 v47, v56, v57
	v_lshl_add_u64 v[60:61], v[34:35], 0, v[194:195]
	v_cvt_pk_bf16_f32 v46, v58, v59
	v_cvt_pk_bf16_f32 v44, v50, v51
	global_store_dwordx4 v[60:61], v[44:47], off
	v_lshl_add_u64 v[34:35], v[34:35], 0, v[40:41]
	s_nop 0
	v_pk_mul_f32 v[46:47], v[12:13], v[50:51]
	v_pk_mul_f32 v[50:51], v[8:9], v[58:59]
	v_mov_b32_e32 v45, v203
	v_mov_b32_e32 v44, v203
	v_cvt_pk_fp8_f32 v45, v50, v51
	v_cvt_pk_fp8_f32 v44, v46, v47
	v_pk_mul_f32 v[46:47], v[14:15], v[48:49]
	v_pk_mul_f32 v[48:49], v[10:11], v[56:57]
	v_lshlrev_b32_e32 v50, 16, v55
	v_cvt_pk_fp8_f32 v45, v48, v49 op_sel:[0,0,1]
	v_lshlrev_b32_e32 v48, 16, v53
	v_and_b32_e32 v49, 0xffff0000, v53
	v_cvt_pk_fp8_f32 v44, v46, v47 op_sel:[0,0,1]
	v_lshlrev_b32_e32 v46, 16, v52
	v_and_b32_e32 v47, 0xffff0000, v52
	v_pk_fma_f32 v[52:53], v[86:87], s[46:47], v[48:49] op_sel_hi:[1,0,1]
	v_lshlrev_b32_e32 v48, 16, v54
	v_and_b32_e32 v49, 0xffff0000, v54
	v_pk_fma_f32 v[46:47], v[84:85], s[46:47], v[46:47] op_sel_hi:[1,0,1]
	v_and_b32_e32 v51, 0xffff0000, v55
	v_pk_fma_f32 v[56:57], v[80:81], s[46:47], v[48:49] op_sel_hi:[1,0,1]
	v_pk_fma_f32 v[54:55], v[82:83], s[46:47], v[50:51] op_sel_hi:[1,0,1]
	v_cvt_pk_bf16_f32 v48, v46, v47
	v_cvt_pk_bf16_f32 v50, v56, v57
	v_pk_mul_f32 v[58:59], v[4:5], v[46:47]
	v_pk_mul_f32 v[56:57], v[0:1], v[56:57]
	v_mov_b32_e32 v46, v203
	v_mov_b32_e32 v47, v203
	v_cvt_pk_fp8_f32 v46, v58, v59
	v_cvt_pk_fp8_f32 v47, v56, v57
	v_cvt_pk_bf16_f32 v49, v52, v53
	v_cvt_pk_bf16_f32 v51, v54, v55
	v_pk_mul_f32 v[52:53], v[6:7], v[52:53]
	v_pk_mul_f32 v[54:55], v[2:3], v[54:55]
	v_cvt_pk_fp8_f32 v46, v52, v53 op_sel:[0,0,1]
	v_cvt_pk_fp8_f32 v47, v54, v55 op_sel:[0,0,1]
	global_store_dwordx4 v[60:61], v[48:51], off offset:16
	s_nop 1
	v_lshl_add_u64 v[48:49], s[42:43], 0, v[192:193]
	v_lshl_add_u64 v[48:49], v[48:49], 0, v[32:33]
	global_store_dwordx4 v[48:49], v[44:47], off
	s_waitcnt vmcnt(8)
	s_nop 0
	v_lshlrev_b32_e32 v44, 16, v28
	v_and_b32_e32 v45, 0xffff0000, v28
	v_lshlrev_b32_e32 v28, 16, v29
	v_and_b32_e32 v29, 0xffff0000, v29
	v_pk_fma_f32 v[46:47], v[110:111], s[46:47], v[28:29] op_sel_hi:[1,0,1]
	v_lshlrev_b32_e32 v28, 16, v30
	v_and_b32_e32 v29, 0xffff0000, v30
	v_lshlrev_b32_e32 v30, 16, v31
	v_and_b32_e32 v31, 0xffff0000, v31
	v_pk_fma_f32 v[44:45], v[108:109], s[46:47], v[44:45] op_sel_hi:[1,0,1]
	v_pk_fma_f32 v[48:49], v[106:107], s[46:47], v[30:31] op_sel_hi:[1,0,1]
	v_pk_fma_f32 v[50:51], v[104:105], s[46:47], v[28:29] op_sel_hi:[1,0,1]
	v_cvt_pk_bf16_f32 v28, v44, v45
	v_cvt_pk_bf16_f32 v31, v48, v49
	v_cvt_pk_bf16_f32 v29, v46, v47
	s_nop 0
	v_cvt_pk_bf16_f32 v30, v50, v51
	global_store_dwordx4 v[42:43], v[28:31], off
	s_nop 1
	v_pk_mul_f32 v[30:31], v[12:13], v[44:45]
	v_mov_b32_e32 v28, v203
	v_pk_mul_f32 v[44:45], v[8:9], v[50:51]
	v_cvt_pk_fp8_f32 v28, v30, v31
	v_mov_b32_e32 v29, v203
	v_cvt_pk_fp8_f32 v29, v44, v45
	v_pk_mul_f32 v[30:31], v[14:15], v[46:47]
	v_pk_mul_f32 v[44:45], v[10:11], v[48:49]
	v_cvt_pk_fp8_f32 v28, v30, v31 op_sel:[0,0,1]
	v_lshlrev_b32_e32 v30, 16, v24
	v_and_b32_e32 v31, 0xffff0000, v24
	v_lshlrev_b32_e32 v24, 16, v25
	v_and_b32_e32 v25, 0xffff0000, v25
	v_cvt_pk_fp8_f32 v29, v44, v45 op_sel:[0,0,1]
	v_pk_fma_f32 v[44:45], v[78:79], s[46:47], v[24:25] op_sel_hi:[1,0,1]
	v_lshlrev_b32_e32 v24, 16, v26
	v_and_b32_e32 v25, 0xffff0000, v26
	v_pk_fma_f32 v[30:31], v[76:77], s[46:47], v[30:31] op_sel_hi:[1,0,1]
	v_lshlrev_b32_e32 v26, 16, v27
	v_and_b32_e32 v27, 0xffff0000, v27
	v_pk_fma_f32 v[48:49], v[72:73], s[46:47], v[24:25] op_sel_hi:[1,0,1]
	v_pk_fma_f32 v[46:47], v[74:75], s[46:47], v[26:27] op_sel_hi:[1,0,1]
	v_cvt_pk_bf16_f32 v24, v30, v31
	v_cvt_pk_bf16_f32 v26, v48, v49
	v_pk_mul_f32 v[50:51], v[4:5], v[30:31]
	v_pk_mul_f32 v[48:49], v[0:1], v[48:49]
	v_mov_b32_e32 v30, v203
	v_mov_b32_e32 v31, v203
	v_cvt_pk_fp8_f32 v30, v50, v51
	v_cvt_pk_fp8_f32 v31, v48, v49
	v_cvt_pk_bf16_f32 v25, v44, v45
	v_cvt_pk_bf16_f32 v27, v46, v47
	v_pk_mul_f32 v[44:45], v[6:7], v[44:45]
	v_pk_mul_f32 v[46:47], v[2:3], v[46:47]
	v_cvt_pk_fp8_f32 v30, v44, v45 op_sel:[0,0,1]
	v_cvt_pk_fp8_f32 v31, v46, v47 op_sel:[0,0,1]
	global_store_dwordx4 v[42:43], v[24:27], off offset:16
	s_nop 1
	v_lshl_add_u64 v[24:25], s[42:43], 0, v[38:39]
	v_lshl_add_u64 v[24:25], v[24:25], 0, v[32:33]
	global_store_dwordx4 v[24:25], v[28:31], off
	s_waitcnt vmcnt(9)
	v_lshlrev_b32_e32 v24, 16, v20
	v_and_b32_e32 v25, 0xffff0000, v20
	v_lshlrev_b32_e32 v20, 16, v21
	v_and_b32_e32 v21, 0xffff0000, v21
	v_pk_fma_f32 v[26:27], v[102:103], s[46:47], v[20:21] op_sel_hi:[1,0,1]
	v_lshlrev_b32_e32 v20, 16, v22
	v_and_b32_e32 v21, 0xffff0000, v22
	v_pk_fma_f32 v[24:25], v[100:101], s[46:47], v[24:25] op_sel_hi:[1,0,1]
	v_lshlrev_b32_e32 v22, 16, v23
	v_and_b32_e32 v23, 0xffff0000, v23
	v_pk_fma_f32 v[30:31], v[96:97], s[46:47], v[20:21] op_sel_hi:[1,0,1]
	v_cvt_pk_bf16_f32 v20, v24, v25
	v_cvt_pk_bf16_f32 v21, v26, v27
	v_pk_fma_f32 v[28:29], v[98:99], s[46:47], v[22:23] op_sel_hi:[1,0,1]
	v_cvt_pk_bf16_f32 v22, v30, v31
	v_pk_mul_f32 v[12:13], v[12:13], v[24:25]
	v_cvt_pk_bf16_f32 v23, v28, v29
	global_store_dwordx4 v[34:35], v[20:23], off
	v_pk_mul_f32 v[10:11], v[10:11], v[28:29]
	s_nop 0
	v_pk_mul_f32 v[20:21], v[8:9], v[30:31]
	v_mov_b32_e32 v8, v203
	v_cvt_pk_fp8_f32 v8, v12, v13
	v_mov_b32_e32 v9, v203
	v_cvt_pk_fp8_f32 v9, v20, v21
	v_pk_mul_f32 v[12:13], v[14:15], v[26:27]
	v_lshlrev_b32_e32 v14, 16, v19
	v_cvt_pk_fp8_f32 v8, v12, v13 op_sel:[0,0,1]
	v_lshlrev_b32_e32 v12, 16, v17
	v_and_b32_e32 v13, 0xffff0000, v17
	v_cvt_pk_fp8_f32 v9, v10, v11 op_sel:[0,0,1]
	v_lshlrev_b32_e32 v10, 16, v16
	v_and_b32_e32 v11, 0xffff0000, v16
	v_pk_fma_f32 v[16:17], v[70:71], s[46:47], v[12:13] op_sel_hi:[1,0,1]
	v_lshlrev_b32_e32 v12, 16, v18
	v_and_b32_e32 v13, 0xffff0000, v18
	v_pk_fma_f32 v[10:11], v[68:69], s[46:47], v[10:11] op_sel_hi:[1,0,1]
	v_pk_fma_f32 v[20:21], v[64:65], s[46:47], v[12:13] op_sel_hi:[1,0,1]
	v_cvt_pk_bf16_f32 v12, v10, v11
	v_pk_mul_f32 v[4:5], v[4:5], v[10:11]
	v_pk_mul_f32 v[0:1], v[0:1], v[20:21]
	v_mov_b32_e32 v10, v203
	v_mov_b32_e32 v11, v203
	v_cvt_pk_fp8_f32 v10, v4, v5
	v_cvt_pk_fp8_f32 v11, v0, v1
	v_and_b32_e32 v15, 0xffff0000, v19
	v_pk_fma_f32 v[18:19], v[66:67], s[46:47], v[14:15] op_sel_hi:[1,0,1]
	v_pk_mul_f32 v[0:1], v[6:7], v[16:17]
	v_pk_mul_f32 v[2:3], v[2:3], v[18:19]
	v_cvt_pk_fp8_f32 v10, v0, v1 op_sel:[0,0,1]
	v_cvt_pk_fp8_f32 v11, v2, v3 op_sel:[0,0,1]
	v_lshl_add_u64 v[0:1], s[42:43], 0, v[36:37]
	v_lshl_add_u64 v[0:1], v[0:1], 0, v[32:33]
	v_cvt_pk_bf16_f32 v13, v16, v17
	v_cvt_pk_bf16_f32 v14, v20, v21
	v_cvt_pk_bf16_f32 v15, v18, v19
	global_store_dwordx4 v[34:35], v[12:15], off offset:16
	global_store_dwordx4 v[0:1], v[8:11], off
	s_and_b64 vcc, exec, s[0:1]
	s_mov_b64 s[0:1], -1
	s_cbranch_vccnz .LBB0_908
	v_readlane_b32 s0, v249, 8
	v_readlane_b32 s1, v249, 9
	s_andn2_b64 vcc, exec, s[0:1]
	s_cbranch_vccnz .LBB0_907
	s_barrier
	s_branch .LBB0_907
